# GEMM phase prologues: K-tile 1 stage loads issued before the first wait (vmcnt(2)->vmcnt(8)), on top of v36
# speedup vs baseline: 1.0185x; 1.0000x over previous
; #define PG8_STAGE(bufoff, gbase, voff) do { _Pragma("unroll") for (int _i = 0; _i < 2; ++_i) \
;         __builtin_amdgcn_global_load_lds((const unsigned*)((const char*)(gbase) + (voff)[_i]), (PG8_LAS unsigned*)(lds + (bufoff) + ldsw + _i * 8192), 16, 0, 0); } while (0)
; #define PG8_WAIT_V(n) asm volatile("s_waitcnt vmcnt(" #n ")" ::: "memory")
; #define PG8_BAR __builtin_amdgcn_s_barrier()
;     ...
;         PG8_STAGE(PG8_SB(0, 0), cB, voffB); PG8_STAGE(PG8_SB(0, 1), cB + hstep, voffB); PG8_STAGE(PG8_SA(0, 0), cA, voffA); PG8_STAGE(PG8_SA(0, 1), cA + hstepA, voffA);
;         if (wr == 1) PG8_BAR;
;         PG8_WAIT_V(2); PG8_BAR;
;         PG8_STAGE(PG8_SB(1, 0), cB + kstep, voffB); PG8_STAGE(PG8_SA(1, 0), cA + PG8_KA(1), voffA); PG8_STAGE(PG8_SB(1, 1), cB + hstep + kstep, voffB);
;         PG8_WAIT_V(6); PG8_BAR;
.LBB0_141:
	s_add_i32 s17, s9, 0x18000
	s_mov_b64 s[4:5], 0x80
	v_lshl_add_u64 v[8:9], v[8:9], 0, s[4:5]
	s_mov_b32 m0, s17
	s_add_i32 s18, s9, 0x1a000
	s_lshl_b32 s26, s23, 13
	global_load_lds_dwordx4 v[8:9], off
	v_lshl_add_u64 v[6:7], v[6:7], 0, s[4:5]
	s_mov_b32 m0, s18
	s_add_i32 s19, s9, 0x8000
	s_add_i32 s20, s9, 0xa000
	global_load_lds_dwordx4 v[6:7], off
	v_lshl_add_u64 v[2:3], v[2:3], 0, s[4:5]
	s_mov_b32 m0, s19
	s_add_u32 s24, s88, 0x40080
	global_load_lds_dwordx4 v[2:3], off
	v_lshl_add_u64 v[2:3], v[4:5], 0, s[4:5]
	s_mov_b32 m0, s20
	s_addc_u32 s25, s89, 0
	s_add_i32 s21, s9, 0x1c000
	global_load_lds_dwordx4 v[2:3], off
	v_lshl_add_u64 v[2:3], s[24:25], 0, v[166:167]
	s_mov_b32 m0, s21
	s_add_i32 s33, s9, 0x1e000
	global_load_lds_dwordx4 v[2:3], off
	v_lshl_add_u64 v[2:3], s[24:25], 0, v[168:169]
	s_mov_b32 m0, s33
	v_lshlrev_b32_e32 v5, 11, v204
	global_load_lds_dwordx4 v[2:3], off
	s_waitcnt vmcnt(8)
	s_barrier
	v_lshlrev_b32_e32 v3, 2, v207
	v_lshl_or_b32 v2, v207, 6, v208
	v_and_b32_e32 v3, 32, v3
	v_xad_u32 v4, v2, v3, 0
	v_lshlrev_b32_e32 v2, 8, v0
	v_and_b32_e32 v2, 0x18000, v2
	v_or3_b32 v2, v1, v2, v5
	s_mov_b64 s[24:25], 0x40080
	v_add_u32_e32 v2, v2, v203
	v_mov_b32_e32 v3, v167
	v_lshl_add_u64 v[138:139], v[2:3], 0, s[24:25]
	v_lshlrev_b32_e32 v2, 4, v205
	v_and_b32_e32 v2, 0x38000, v2
	s_waitcnt vmcnt(6)
	v_or3_b32 v2, v1, v2, v5
	s_cmpk_lt_u32 s7, 0x100
	v_add_u32_e32 v2, v2, v203
	s_sext_i32_i16 s85, s6
	v_lshl_or_b32 v160, s23, 6, v207
	s_mov_b32 s37, 0
	s_cselect_b64 s[48:49], -1, 0
	v_or_b32_e32 v161, s22, v206
	v_lshl_add_u64 v[140:141], v[2:3], 0, s[24:25]
	v_mov_b64_e32 v[142:143], 0x600
	v_mov_b64_e32 v[144:145], 0x5ff
	v_add_u32_e32 v162, 0, v10
	v_add_u32_e32 v163, s26, v4
	s_movk_i32 s63, 0x3000
	s_barrier
	s_branch .LBB0_144

; #define PG8_STAGE(bufoff, gbase, voff) do { _Pragma("unroll") for (int _i = 0; _i < 2; ++_i) \
;         __builtin_amdgcn_global_load_lds((const unsigned*)((const char*)(gbase) + (voff)[_i]), (PG8_LAS unsigned*)(lds + (bufoff) + ldsw + _i * 8192), 16, 0, 0); } while (0)
; #define PG8_WAIT_V(n) asm volatile("s_waitcnt vmcnt(" #n ")" ::: "memory")
; #define PG8_BAR __builtin_amdgcn_s_barrier()
;     ...
;         PG8_STAGE(PG8_SB(0, 0), cB, voffB); PG8_STAGE(PG8_SB(0, 1), cB + hstep, voffB); PG8_STAGE(PG8_SA(0, 0), cA, voffA); PG8_STAGE(PG8_SA(0, 1), cA + hstepA, voffA);
;         if (wr == 1) PG8_BAR;
;         PG8_WAIT_V(2); PG8_BAR;
;         PG8_STAGE(PG8_SB(1, 0), cB + kstep, voffB); PG8_STAGE(PG8_SA(1, 0), cA + PG8_KA(1), voffA); PG8_STAGE(PG8_SB(1, 1), cB + hstep + kstep, voffB);
;         PG8_WAIT_V(6); PG8_BAR;
.LBB0_470:
	s_add_i32 s19, s10, 0x18000
	s_mov_b64 s[46:47], 0x80
	v_lshl_add_u64 v[8:9], v[8:9], 0, s[46:47]
	s_mov_b32 m0, s19
	s_add_i32 s33, s10, 0x1a000
	s_lshl_b32 s21, s5, 13
	global_load_lds_dwordx4 v[8:9], off
	v_lshl_add_u64 v[4:5], v[4:5], 0, s[46:47]
	s_mov_b32 m0, s33
	s_add_i32 s37, s10, 0x8000
	s_add_i32 s53, s10, 0xa000
	global_load_lds_dwordx4 v[4:5], off
	v_lshl_add_u64 v[2:3], v[2:3], 0, s[46:47]
	s_mov_b32 m0, s37
	s_add_u32 s22, s76, 0x40080
	global_load_lds_dwordx4 v[2:3], off
	v_lshl_add_u64 v[2:3], v[6:7], 0, s[46:47]
	s_mov_b32 m0, s53
	s_addc_u32 s23, s77, 0
	s_add_i32 s63, s10, 0x1c000
	global_load_lds_dwordx4 v[2:3], off
	v_lshl_add_u64 v[2:3], s[22:23], 0, v[166:167]
	s_mov_b32 m0, s63
	s_add_i32 s67, s10, 0x1e000
	global_load_lds_dwordx4 v[2:3], off
	v_lshl_add_u64 v[2:3], s[22:23], 0, v[168:169]
	s_mov_b32 m0, s67
	v_lshlrev_b32_e32 v5, 11, v204
	global_load_lds_dwordx4 v[2:3], off
	s_waitcnt vmcnt(8)
	s_barrier
	v_lshlrev_b32_e32 v2, 8, v0
	v_and_b32_e32 v2, 0x18000, v2
	v_or3_b32 v2, v1, v2, v5
	v_lshl_or_b32 v186, s5, 6, v207
	s_sext_i32_i8 s6, s4
	s_mov_b64 s[4:5], 0x40080
	v_add_u32_e32 v2, v2, v203
	v_mov_b32_e32 v3, v167
	v_lshl_add_u64 v[162:163], v[2:3], 0, s[4:5]
	v_lshlrev_b32_e32 v2, 4, v205
	v_lshlrev_b32_e32 v12, 2, v207
	v_and_b32_e32 v2, 0x38000, v2
	v_lshl_or_b32 v11, v207, 6, v208
	v_and_b32_e32 v12, 32, v12
	s_waitcnt vmcnt(6)
	v_or3_b32 v2, v1, v2, v5
	v_xad_u32 v4, v11, v12, 0
	s_cmpk_lt_u32 s20, 0x100
	v_add_u32_e32 v2, v2, v203
	s_cselect_b64 s[48:49], -1, 0
	v_or_b32_e32 v187, s7, v206
	v_lshl_add_u64 v[164:165], v[2:3], 0, s[4:5]
	v_mov_b64_e32 v[174:175], 0x200
	v_mov_b64_e32 v[176:177], 0x1ff
	v_add_u32_e32 v188, 0, v10
	v_add_u32_e32 v189, s21, v4
	s_mov_b32 s52, 0x3f9837f0
	s_barrier
	s_branch .LBB0_473

; #define PG8_STAGE(bufoff, gbase, voff) do { _Pragma("unroll") for (int _i = 0; _i < 2; ++_i) \
;         __builtin_amdgcn_global_load_lds((const unsigned*)((const char*)(gbase) + (voff)[_i]), (PG8_LAS unsigned*)(lds + (bufoff) + ldsw + _i * 8192), 16, 0, 0); } while (0)
; #define PG8_WAIT_V(n) asm volatile("s_waitcnt vmcnt(" #n ")" ::: "memory")
; #define PG8_BAR __builtin_amdgcn_s_barrier()
;     ...
;         PG8_STAGE(PG8_SB(0, 0), cB, voffB); PG8_STAGE(PG8_SB(0, 1), cB + hstep, voffB); PG8_STAGE(PG8_SA(0, 0), cA, voffA); PG8_STAGE(PG8_SA(0, 1), cA + hstepA, voffA);
;         if (wr == 1) PG8_BAR;
;         PG8_WAIT_V(2); PG8_BAR;
;         PG8_STAGE(PG8_SB(1, 0), cB + kstep, voffB); PG8_STAGE(PG8_SA(1, 0), cA + PG8_KA(1), voffA); PG8_STAGE(PG8_SB(1, 1), cB + hstep + kstep, voffB);
;         PG8_WAIT_V(6); PG8_BAR;
.LBB0_616:
	s_sext_i32_i8 s63, s4
	v_lshl_or_b32 v160, s5, 6, v207
	s_lshl_b32 s24, s5, 13
	s_add_i32 s19, s10, 0x18000
	s_mov_b64 s[4:5], 0x80
	v_lshl_add_u64 v[8:9], v[8:9], 0, s[4:5]
	s_mov_b32 m0, s19
	s_add_i32 s20, s10, 0x1a000
	global_load_lds_dwordx4 v[8:9], off
	v_lshl_add_u64 v[6:7], v[6:7], 0, s[4:5]
	s_mov_b32 m0, s20
	s_add_i32 s21, s10, 0x8000
	s_add_i32 s33, s10, 0xa000
	global_load_lds_dwordx4 v[6:7], off
	v_lshl_add_u64 v[2:3], v[2:3], 0, s[4:5]
	s_mov_b32 m0, s21
	s_add_u32 s22, s58, 0x40080
	global_load_lds_dwordx4 v[2:3], off
	v_lshl_add_u64 v[2:3], v[4:5], 0, s[4:5]
	s_mov_b32 m0, s33
	s_addc_u32 s23, s59, 0
	s_add_i32 s37, s10, 0x1c000
	global_load_lds_dwordx4 v[2:3], off
	v_lshl_add_u64 v[2:3], s[22:23], 0, v[166:167]
	s_mov_b32 m0, s37
	s_add_i32 s55, s10, 0x1e000
	global_load_lds_dwordx4 v[2:3], off
	v_lshl_add_u64 v[2:3], s[22:23], 0, v[168:169]
	s_mov_b32 m0, s55
	v_lshlrev_b32_e32 v5, 8, v204
	global_load_lds_dwordx4 v[2:3], off
	s_waitcnt vmcnt(8)
	s_barrier
	v_lshlrev_b32_e32 v2, 5, v0
	v_and_b32_e32 v2, 0x3000, v2
	v_or3_b32 v2, v1, v2, v5
	s_cmpk_lt_u32 s7, 0x100
	v_or_b32_e32 v161, s6, v206
	v_add_u32_e32 v2, v2, v203
	v_mov_b32_e32 v3, v167
	s_mov_b64 s[6:7], 0x8080
	v_lshl_add_u64 v[142:143], v[2:3], 0, s[6:7]
	v_lshlrev_b32_e32 v2, 1, v205
	v_lshlrev_b32_e32 v12, 2, v207
	v_and_b32_e32 v2, 0x7000, v2
	v_lshl_or_b32 v11, v207, 6, v208
	v_and_b32_e32 v12, 32, v12
	s_waitcnt vmcnt(6)
	v_or3_b32 v1, v1, v2, v5
	v_xad_u32 v4, v11, v12, 0
	v_add_u32_e32 v2, v1, v203
	s_cselect_b64 s[42:43], -1, 0
	v_lshl_add_u64 v[144:145], v[2:3], 0, s[6:7]
	v_mov_b64_e32 v[146:147], 0x200
	v_mov_b64_e32 v[148:149], 0x1ff
	v_add_u32_e32 v1, 0, v10
	v_add_u32_e32 v162, s24, v4
	s_barrier
	s_branch .LBB0_619
